# in-phase weight prep: fp8 / bf16 conversion loops handle four chunks per round trip (loads of four chunks in flight behind counted waits) instead of one; assumes 1024 prep waves (128 workgroups)
# speedup vs baseline: 1.0391x; 1.0056x over previous
; __device__ __forceinline__ void cvt8_chunk(const float* src, unsigned char* dst, size_t chunk, int lane, float sc) {
;     const f32x4* s = (const f32x4*)(src + chunk * 512) + lane * 2; const f32x4 a = s[0] * sc, b = s[1] * sc;
;     int w0 = 0, w1 = 0;
;     w0 = __builtin_amdgcn_cvt_pk_fp8_f32(a.x, a.y, w0, false); w0 = __builtin_amdgcn_cvt_pk_fp8_f32(a.z, a.w, w0, true);
;     w1 = __builtin_amdgcn_cvt_pk_fp8_f32(b.x, b.y, w1, false); w1 = __builtin_amdgcn_cvt_pk_fp8_f32(b.z, b.w, w1, true);
;     *(v2u*)(dst + chunk * 512 + lane * 8) = (v2u){(unsigned)w0, (unsigned)w1};
; }
; __device__ __forceinline__ void prep_phase(Frame& F, const Args& a, int layer, int blk, int nblk_, int part) {
;     ...
;         for (int it = gw; it < ntot; it += NGW) {
;             int r = it;
;             if (r < n2) { cvt8_chunk(ut, (unsigned char*)(db + DB_U), r, lane, 256.f); continue; } r -= n2;
;             if (r < n2) { cvt8_chunk(vt, (unsigned char*)(db + DB_V), r, lane, 64.f); continue; } r -= n2;
.LBB0_1194:
	v_lshl_add_u64 v[6:7], v[2:3], 4, s[36:37]
	s_lshl_b64 s[36:37], s[22:23], 9
	s_lshl_b64 s[22:23], s[22:23], 11
	v_lshl_add_u64 v[150:151], v[6:7], 0, s[22:23]
	v_lshl_add_u64 v[14:15], v[4:5], 0, s[38:39]
	global_load_dwordx4 v[104:107], v[150:151], off offset:16
	global_load_dwordx4 v[100:103], v[150:151], off
	v_add_co_u32_e32 v150, vcc, 0x200000, v150
	s_nop 1
	v_addc_co_u32_e32 v151, vcc, 0, v151, vcc
	global_load_dwordx4 v[112:115], v[150:151], off offset:16
	global_load_dwordx4 v[108:111], v[150:151], off
	v_add_co_u32_e32 v150, vcc, 0x200000, v150
	s_nop 1
	v_addc_co_u32_e32 v151, vcc, 0, v151, vcc
	global_load_dwordx4 v[120:123], v[150:151], off offset:16
	global_load_dwordx4 v[116:119], v[150:151], off
	v_add_co_u32_e32 v150, vcc, 0x200000, v150
	s_nop 1
	v_addc_co_u32_e32 v151, vcc, 0, v151, vcc
	global_load_dwordx4 v[128:131], v[150:151], off offset:16
	global_load_dwordx4 v[124:127], v[150:151], off
	v_lshl_add_u64 v[148:149], v[14:15], 0, s[36:37]
	s_waitcnt vmcnt(6)
	v_mov_b32_e32 v132, v0
	v_mov_b32_e32 v133, v0
	v_pk_mul_f32 v[104:105], v[104:105], s[20:21] op_sel_hi:[1,0]
	v_pk_mul_f32 v[100:101], v[100:101], s[20:21] op_sel_hi:[1,0]
	v_cvt_pk_fp8_f32 v133, v104, v105
	v_cvt_pk_fp8_f32 v132, v100, v101
	v_pk_mul_f32 v[102:103], v[102:103], s[20:21] op_sel_hi:[1,0]
	v_pk_mul_f32 v[106:107], v[106:107], s[20:21] op_sel_hi:[1,0]
	v_cvt_pk_fp8_f32 v132, v102, v103 op_sel:[0,0,1]
	v_cvt_pk_fp8_f32 v133, v106, v107 op_sel:[0,0,1]
	global_store_dwordx2 v[148:149], v[132:133], off
	s_waitcnt vmcnt(5)
	v_mov_b32_e32 v134, v0
	v_mov_b32_e32 v135, v0
	v_pk_mul_f32 v[112:113], v[112:113], s[20:21] op_sel_hi:[1,0]
	v_pk_mul_f32 v[108:109], v[108:109], s[20:21] op_sel_hi:[1,0]
	v_cvt_pk_fp8_f32 v135, v112, v113
	v_cvt_pk_fp8_f32 v134, v108, v109
	v_pk_mul_f32 v[110:111], v[110:111], s[20:21] op_sel_hi:[1,0]
	v_pk_mul_f32 v[114:115], v[114:115], s[20:21] op_sel_hi:[1,0]
	v_cvt_pk_fp8_f32 v134, v110, v111 op_sel:[0,0,1]
	v_cvt_pk_fp8_f32 v135, v114, v115 op_sel:[0,0,1]
	v_add_co_u32_e32 v148, vcc, 0x80000, v148
	s_nop 1
	v_addc_co_u32_e32 v149, vcc, 0, v149, vcc
	global_store_dwordx2 v[148:149], v[134:135], off
	s_waitcnt vmcnt(4)
	v_mov_b32_e32 v136, v0
	v_mov_b32_e32 v137, v0
	v_pk_mul_f32 v[120:121], v[120:121], s[20:21] op_sel_hi:[1,0]
	v_pk_mul_f32 v[116:117], v[116:117], s[20:21] op_sel_hi:[1,0]
	v_cvt_pk_fp8_f32 v137, v120, v121
	v_cvt_pk_fp8_f32 v136, v116, v117
	v_pk_mul_f32 v[118:119], v[118:119], s[20:21] op_sel_hi:[1,0]
	v_pk_mul_f32 v[122:123], v[122:123], s[20:21] op_sel_hi:[1,0]
	v_cvt_pk_fp8_f32 v136, v118, v119 op_sel:[0,0,1]
	v_cvt_pk_fp8_f32 v137, v122, v123 op_sel:[0,0,1]
	v_add_co_u32_e32 v148, vcc, 0x80000, v148
	s_nop 1
	v_addc_co_u32_e32 v149, vcc, 0, v149, vcc
	global_store_dwordx2 v[148:149], v[136:137], off
	s_waitcnt vmcnt(3)
	v_mov_b32_e32 v138, v0
	v_mov_b32_e32 v139, v0
	v_pk_mul_f32 v[128:129], v[128:129], s[20:21] op_sel_hi:[1,0]
	v_pk_mul_f32 v[124:125], v[124:125], s[20:21] op_sel_hi:[1,0]
	v_cvt_pk_fp8_f32 v139, v128, v129
	v_cvt_pk_fp8_f32 v138, v124, v125
	v_pk_mul_f32 v[126:127], v[126:127], s[20:21] op_sel_hi:[1,0]
	v_pk_mul_f32 v[130:131], v[130:131], s[20:21] op_sel_hi:[1,0]
	v_cvt_pk_fp8_f32 v138, v126, v127 op_sel:[0,0,1]
	v_cvt_pk_fp8_f32 v139, v130, v131 op_sel:[0,0,1]
	v_add_co_u32_e32 v148, vcc, 0x80000, v148
	s_nop 1
	v_addc_co_u32_e32 v149, vcc, 0, v149, vcc
	global_store_dwordx2 v[148:149], v[138:139], off
	v_readlane_b32 s20, v254, 44
	v_readlane_b32 s21, v254, 45
	s_lshl_b64 s[20:21], s[20:21], 2
	s_add_u32 s2, s2, s20
	s_addc_u32 s3, s3, s21
	s_cmp_lt_i32 s2, 0x10000
	s_cbranch_scc0 .LBB0_1197

; __device__ __forceinline__ u32x4 pk8(const f32x4 a, const f32x4 b) { u32x4 w; w.x = cvt_pk_bf16(a[0], a[1]); w.y = cvt_pk_bf16(a[2], a[3]); w.z = cvt_pk_bf16(b[0], b[1]); w.w = cvt_pk_bf16(b[2], b[3]); return w; }
; __device__ __forceinline__ void cvt_chunk(const float* src, bf16* dst, size_t chunk, int lane) {
;     const f32x4* s = (const f32x4*)(src + chunk * 512) + lane * 2; const f32x4 a = s[0], b = s[1];
;     *(v4u*)(dst + chunk * 512 + lane * 8) = pk8(a, b);
; }
; __device__ __forceinline__ void prep_phase(Frame& F, const Args& a, int layer, int blk, int nblk_, int part) {
;     ...
;             if (r < n4) { cvt_chunk(pin, (bf16*)(db + DB_PB), r, lane); continue; } r -= n4;
.LBB0_1300:
	s_andn2_b64 vcc, exec, s[22:23]
	s_cbranch_vccnz .LBB0_1302
	s_add_i32 s22, s5, 0x8000
	s_and_b32 s22, s22, 0xc00
	s_cmp_lg_u32 s22, 0
	s_cbranch_scc1 .LBB0_1302
	v_readlane_b32 s22, v254, 30
	s_add_i32 s22, s22, s36
	s_add_i32 s30, s22, 0xfe000000
	v_lshl_add_u64 v[150:151], s[30:31], 2, v[10:11]
	global_load_dwordx4 v[100:103], v[150:151], off
	global_load_dwordx4 v[104:107], v[150:151], off offset:16
	v_add_co_u32_e32 v150, vcc, 0x200000, v150
	s_nop 1
	v_addc_co_u32_e32 v151, vcc, 0, v151, vcc
	global_load_dwordx4 v[108:111], v[150:151], off
	global_load_dwordx4 v[112:115], v[150:151], off offset:16
	v_add_co_u32_e32 v150, vcc, 0x200000, v150
	s_nop 1
	v_addc_co_u32_e32 v151, vcc, 0, v151, vcc
	global_load_dwordx4 v[116:119], v[150:151], off
	global_load_dwordx4 v[120:123], v[150:151], off offset:16
	v_add_co_u32_e32 v150, vcc, 0x200000, v150
	s_nop 1
	v_addc_co_u32_e32 v151, vcc, 0, v151, vcc
	global_load_dwordx4 v[124:127], v[150:151], off
	global_load_dwordx4 v[128:131], v[150:151], off offset:16
	v_lshl_add_u64 v[148:149], s[30:31], 1, v[12:13]
	s_waitcnt vmcnt(6)
	v_cvt_pk_bf16_f32 v100, v100, v101
	v_cvt_pk_bf16_f32 v101, v102, v103
	v_cvt_pk_bf16_f32 v102, v104, v105
	v_cvt_pk_bf16_f32 v103, v106, v107
	global_store_dwordx4 v[148:149], v[100:103], off
	s_waitcnt vmcnt(5)
	v_cvt_pk_bf16_f32 v108, v108, v109
	v_cvt_pk_bf16_f32 v109, v110, v111
	v_cvt_pk_bf16_f32 v110, v112, v113
	v_cvt_pk_bf16_f32 v111, v114, v115
	v_add_co_u32_e32 v148, vcc, 0x100000, v148
	s_nop 1
	v_addc_co_u32_e32 v149, vcc, 0, v149, vcc
	global_store_dwordx4 v[148:149], v[108:111], off
	s_waitcnt vmcnt(4)
	v_cvt_pk_bf16_f32 v116, v116, v117
	v_cvt_pk_bf16_f32 v117, v118, v119
	v_cvt_pk_bf16_f32 v118, v120, v121
	v_cvt_pk_bf16_f32 v119, v122, v123
	v_add_co_u32_e32 v148, vcc, 0x100000, v148
	s_nop 1
	v_addc_co_u32_e32 v149, vcc, 0, v149, vcc
	global_store_dwordx4 v[148:149], v[116:119], off
	s_waitcnt vmcnt(3)
	v_cvt_pk_bf16_f32 v124, v124, v125
	v_cvt_pk_bf16_f32 v125, v126, v127
	v_cvt_pk_bf16_f32 v126, v128, v129
	v_cvt_pk_bf16_f32 v127, v130, v131
	v_add_co_u32_e32 v148, vcc, 0x100000, v148
	s_nop 1
	v_addc_co_u32_e32 v149, vcc, 0, v149, vcc
	global_store_dwordx4 v[148:149], v[124:127], off

; __device__ __forceinline__ void cvt8_chunk(const float* src, unsigned char* dst, size_t chunk, int lane, float sc) {
;     const f32x4* s = (const f32x4*)(src + chunk * 512) + lane * 2; const f32x4 a = s[0] * sc, b = s[1] * sc;
;     int w0 = 0, w1 = 0;
;     w0 = __builtin_amdgcn_cvt_pk_fp8_f32(a.x, a.y, w0, false); w0 = __builtin_amdgcn_cvt_pk_fp8_f32(a.z, a.w, w0, true);
;     w1 = __builtin_amdgcn_cvt_pk_fp8_f32(b.x, b.y, w1, false); w1 = __builtin_amdgcn_cvt_pk_fp8_f32(b.z, b.w, w1, true);
;     *(v2u*)(dst + chunk * 512 + lane * 8) = (v2u){(unsigned)w0, (unsigned)w1};
; }
; __device__ __forceinline__ void prep_phase(Frame& F, const Args& a, int layer, int blk, int nblk_, int part) {
;     ...
;             if (r < n2) { cvt8_chunk(vt, (unsigned char*)(db + DB_V), r, lane, 64.f); continue; } r -= n2;
.LBB0_1303:
	s_andn2_b64 vcc, exec, s[22:23]
	s_cbranch_vccnz .LBB0_1305
	s_add_i32 s22, s5, 0x8000
	s_and_b32 s22, s22, 0xc00
	s_cmp_lg_u32 s22, 0
	s_cbranch_scc1 .LBB0_1305
	v_readlane_b32 s22, v254, 30
	s_add_i32 s22, s22, s36
	s_add_i32 s30, s22, 0xff000000
	v_lshl_add_u64 v[150:151], s[30:31], 2, v[14:15]
	s_mov_b32 s22, 0x42800000
	global_load_dwordx4 v[104:107], v[150:151], off offset:16
	global_load_dwordx4 v[100:103], v[150:151], off
	v_add_co_u32_e32 v150, vcc, 0x200000, v150
	s_nop 1
	v_addc_co_u32_e32 v151, vcc, 0, v151, vcc
	global_load_dwordx4 v[112:115], v[150:151], off offset:16
	global_load_dwordx4 v[108:111], v[150:151], off
	v_add_co_u32_e32 v150, vcc, 0x200000, v150
	s_nop 1
	v_addc_co_u32_e32 v151, vcc, 0, v151, vcc
	global_load_dwordx4 v[120:123], v[150:151], off offset:16
	global_load_dwordx4 v[116:119], v[150:151], off
	v_add_co_u32_e32 v150, vcc, 0x200000, v150
	s_nop 1
	v_addc_co_u32_e32 v151, vcc, 0, v151, vcc
	global_load_dwordx4 v[128:131], v[150:151], off offset:16
	global_load_dwordx4 v[124:127], v[150:151], off
	v_lshl_add_u64 v[148:149], v[16:17], 0, s[30:31]
	s_waitcnt vmcnt(6)
	v_mov_b32_e32 v132, v0
	v_mov_b32_e32 v133, v0
	v_pk_mul_f32 v[104:105], v[104:105], s[22:23] op_sel_hi:[1,0]
	v_pk_mul_f32 v[100:101], v[100:101], s[22:23] op_sel_hi:[1,0]
	v_cvt_pk_fp8_f32 v133, v104, v105
	v_cvt_pk_fp8_f32 v132, v100, v101
	v_pk_mul_f32 v[102:103], v[102:103], s[22:23] op_sel_hi:[1,0]
	v_pk_mul_f32 v[106:107], v[106:107], s[22:23] op_sel_hi:[1,0]
	v_cvt_pk_fp8_f32 v132, v102, v103 op_sel:[0,0,1]
	v_cvt_pk_fp8_f32 v133, v106, v107 op_sel:[0,0,1]
	global_store_dwordx2 v[148:149], v[132:133], off
	s_waitcnt vmcnt(5)
	v_mov_b32_e32 v134, v0
	v_mov_b32_e32 v135, v0
	v_pk_mul_f32 v[112:113], v[112:113], s[22:23] op_sel_hi:[1,0]
	v_pk_mul_f32 v[108:109], v[108:109], s[22:23] op_sel_hi:[1,0]
	v_cvt_pk_fp8_f32 v135, v112, v113
	v_cvt_pk_fp8_f32 v134, v108, v109
	v_pk_mul_f32 v[110:111], v[110:111], s[22:23] op_sel_hi:[1,0]
	v_pk_mul_f32 v[114:115], v[114:115], s[22:23] op_sel_hi:[1,0]
	v_cvt_pk_fp8_f32 v134, v110, v111 op_sel:[0,0,1]
	v_cvt_pk_fp8_f32 v135, v114, v115 op_sel:[0,0,1]
	v_add_co_u32_e32 v148, vcc, 0x80000, v148
	s_nop 1
	v_addc_co_u32_e32 v149, vcc, 0, v149, vcc
	global_store_dwordx2 v[148:149], v[134:135], off
	s_waitcnt vmcnt(4)
	v_mov_b32_e32 v136, v0
	v_mov_b32_e32 v137, v0
	v_pk_mul_f32 v[120:121], v[120:121], s[22:23] op_sel_hi:[1,0]
	v_pk_mul_f32 v[116:117], v[116:117], s[22:23] op_sel_hi:[1,0]
	v_cvt_pk_fp8_f32 v137, v120, v121
	v_cvt_pk_fp8_f32 v136, v116, v117
	v_pk_mul_f32 v[118:119], v[118:119], s[22:23] op_sel_hi:[1,0]
	v_pk_mul_f32 v[122:123], v[122:123], s[22:23] op_sel_hi:[1,0]
	v_cvt_pk_fp8_f32 v136, v118, v119 op_sel:[0,0,1]
	v_cvt_pk_fp8_f32 v137, v122, v123 op_sel:[0,0,1]
	v_add_co_u32_e32 v148, vcc, 0x80000, v148
	s_nop 1
	v_addc_co_u32_e32 v149, vcc, 0, v149, vcc
	global_store_dwordx2 v[148:149], v[136:137], off
	s_waitcnt vmcnt(3)
	v_mov_b32_e32 v138, v0
	v_mov_b32_e32 v139, v0
	v_pk_mul_f32 v[128:129], v[128:129], s[22:23] op_sel_hi:[1,0]
	v_pk_mul_f32 v[124:125], v[124:125], s[22:23] op_sel_hi:[1,0]
	v_cvt_pk_fp8_f32 v139, v128, v129
	v_cvt_pk_fp8_f32 v138, v124, v125
	v_pk_mul_f32 v[126:127], v[126:127], s[22:23] op_sel_hi:[1,0]
	v_pk_mul_f32 v[130:131], v[130:131], s[22:23] op_sel_hi:[1,0]
	v_cvt_pk_fp8_f32 v138, v126, v127 op_sel:[0,0,1]
	v_cvt_pk_fp8_f32 v139, v130, v131 op_sel:[0,0,1]
	v_add_co_u32_e32 v148, vcc, 0x80000, v148
	s_nop 1
	v_addc_co_u32_e32 v149, vcc, 0, v149, vcc
	global_store_dwordx2 v[148:149], v[138:139], off

; __device__ __forceinline__ void cvt8_chunk(const float* src, unsigned char* dst, size_t chunk, int lane, float sc) {
;     const f32x4* s = (const f32x4*)(src + chunk * 512) + lane * 2; const f32x4 a = s[0] * sc, b = s[1] * sc;
;     int w0 = 0, w1 = 0;
;     w0 = __builtin_amdgcn_cvt_pk_fp8_f32(a.x, a.y, w0, false); w0 = __builtin_amdgcn_cvt_pk_fp8_f32(a.z, a.w, w0, true);
;     w1 = __builtin_amdgcn_cvt_pk_fp8_f32(b.x, b.y, w1, false); w1 = __builtin_amdgcn_cvt_pk_fp8_f32(b.z, b.w, w1, true);
;     *(v2u*)(dst + chunk * 512 + lane * 8) = (v2u){(unsigned)w0, (unsigned)w1};
; }
; __device__ __forceinline__ void prep_phase(Frame& F, const Args& a, int layer, int blk, int nblk_, int part) {
;     ...
;             if (r < n2) { cvt8_chunk(ut, (unsigned char*)(db + DB_U), r, lane, 256.f); continue; } r -= n2;
.LBB0_1306:
	s_andn2_b64 vcc, exec, s[22:23]
	s_cbranch_vccnz .LBB0_1291
	s_add_i32 s22, s5, 0x8000
	s_and_b32 s22, s22, 0xc00
	s_cmp_lg_u32 s22, 0
	s_cbranch_scc1 .LBB0_1291
	v_lshl_add_u64 v[150:151], s[20:21], 0, v[4:5]
	global_load_dwordx4 v[104:107], v[150:151], off offset:16
	global_load_dwordx4 v[100:103], v[150:151], off
	v_add_co_u32_e32 v150, vcc, 0x200000, v150
	s_nop 1
	v_addc_co_u32_e32 v151, vcc, 0, v151, vcc
	global_load_dwordx4 v[112:115], v[150:151], off offset:16
	global_load_dwordx4 v[108:111], v[150:151], off
	v_add_co_u32_e32 v150, vcc, 0x200000, v150
	s_nop 1
	v_addc_co_u32_e32 v151, vcc, 0, v151, vcc
	global_load_dwordx4 v[120:123], v[150:151], off offset:16
	global_load_dwordx4 v[116:119], v[150:151], off
	v_add_co_u32_e32 v150, vcc, 0x200000, v150
	s_nop 1
	v_addc_co_u32_e32 v151, vcc, 0, v151, vcc
	global_load_dwordx4 v[128:131], v[150:151], off offset:16
	global_load_dwordx4 v[124:127], v[150:151], off
	v_mov_b64_e32 v[148:149], v[2:3]
	s_waitcnt vmcnt(6)
	v_mov_b32_e32 v132, v0
	v_mov_b32_e32 v133, v0
	v_pk_mul_f32 v[104:105], v[104:105], s[8:9] op_sel_hi:[1,0]
	v_pk_mul_f32 v[100:101], v[100:101], s[8:9] op_sel_hi:[1,0]
	v_cvt_pk_fp8_f32 v133, v104, v105
	v_cvt_pk_fp8_f32 v132, v100, v101
	v_pk_mul_f32 v[102:103], v[102:103], s[8:9] op_sel_hi:[1,0]
	v_pk_mul_f32 v[106:107], v[106:107], s[8:9] op_sel_hi:[1,0]
	v_cvt_pk_fp8_f32 v132, v102, v103 op_sel:[0,0,1]
	v_cvt_pk_fp8_f32 v133, v106, v107 op_sel:[0,0,1]
	global_store_dwordx2 v[148:149], v[132:133], off
	s_waitcnt vmcnt(5)
	v_mov_b32_e32 v134, v0
	v_mov_b32_e32 v135, v0
	v_pk_mul_f32 v[112:113], v[112:113], s[8:9] op_sel_hi:[1,0]
	v_pk_mul_f32 v[108:109], v[108:109], s[8:9] op_sel_hi:[1,0]
	v_cvt_pk_fp8_f32 v135, v112, v113
	v_cvt_pk_fp8_f32 v134, v108, v109
	v_pk_mul_f32 v[110:111], v[110:111], s[8:9] op_sel_hi:[1,0]
	v_pk_mul_f32 v[114:115], v[114:115], s[8:9] op_sel_hi:[1,0]
	v_cvt_pk_fp8_f32 v134, v110, v111 op_sel:[0,0,1]
	v_cvt_pk_fp8_f32 v135, v114, v115 op_sel:[0,0,1]
	v_add_co_u32_e32 v148, vcc, 0x80000, v148
	s_nop 1
	v_addc_co_u32_e32 v149, vcc, 0, v149, vcc
	global_store_dwordx2 v[148:149], v[134:135], off
	s_waitcnt vmcnt(4)
	v_mov_b32_e32 v136, v0
	v_mov_b32_e32 v137, v0
	v_pk_mul_f32 v[120:121], v[120:121], s[8:9] op_sel_hi:[1,0]
	v_pk_mul_f32 v[116:117], v[116:117], s[8:9] op_sel_hi:[1,0]
	v_cvt_pk_fp8_f32 v137, v120, v121
	v_cvt_pk_fp8_f32 v136, v116, v117
	v_pk_mul_f32 v[118:119], v[118:119], s[8:9] op_sel_hi:[1,0]
	v_pk_mul_f32 v[122:123], v[122:123], s[8:9] op_sel_hi:[1,0]
	v_cvt_pk_fp8_f32 v136, v118, v119 op_sel:[0,0,1]
	v_cvt_pk_fp8_f32 v137, v122, v123 op_sel:[0,0,1]
	v_add_co_u32_e32 v148, vcc, 0x80000, v148
	s_nop 1
	v_addc_co_u32_e32 v149, vcc, 0, v149, vcc
	global_store_dwordx2 v[148:149], v[136:137], off
	s_waitcnt vmcnt(3)
	v_mov_b32_e32 v138, v0
	v_mov_b32_e32 v139, v0
	v_pk_mul_f32 v[128:129], v[128:129], s[8:9] op_sel_hi:[1,0]
	v_pk_mul_f32 v[124:125], v[124:125], s[8:9] op_sel_hi:[1,0]
	v_cvt_pk_fp8_f32 v139, v128, v129
	v_cvt_pk_fp8_f32 v138, v124, v125
	v_pk_mul_f32 v[126:127], v[126:127], s[8:9] op_sel_hi:[1,0]
	v_pk_mul_f32 v[130:131], v[130:131], s[8:9] op_sel_hi:[1,0]
	v_cvt_pk_fp8_f32 v138, v126, v127 op_sel:[0,0,1]
	v_cvt_pk_fp8_f32 v139, v130, v131 op_sel:[0,0,1]
	v_add_co_u32_e32 v148, vcc, 0x80000, v148
	s_nop 1
	v_addc_co_u32_e32 v149, vcc, 0, v149, vcc
	global_store_dwordx2 v[148:149], v[138:139], off
	s_branch .LBB0_1291
